# final-layer gather: expert ids fetched one group step ahead; the step's only full wait moved from its top to just before the gelu (after the dots and butterfly)
# speedup vs baseline: 1.0136x; 1.0028x over previous
.Lgprio_f:
	v_add_u32_e32 v0, s6, v0
	v_cmp_gt_i32_e32 vcc, s87, v0
	s_and_saveexec_b64 s[6:7], vcc
	s_mov_b32 s18, 0x800000
	s_cbranch_execz .LBB0_765
	v_ashrrev_i32_e32 v1, 31, v0
	v_and_b32_e32 v2, 15, v3
	v_lshlrev_b64 v[34:35], 9, v[0:1]
	v_lshl_add_u64 v[4:5], s[94:95], 0, v[34:35]
	v_lshlrev_b32_e32 v144, 2, v2
	v_lshl_add_u64 v[4:5], v[4:5], 0, v[144:145]
	global_load_dword v92, v[4:5], off
	global_load_dword v122, v[4:5], off offset:64
	v_readlane_b32 s12, v255, 7
	v_readlane_b32 s13, v255, 8
	s_lshl_b64 s[8:9], s[12:13], 17
	s_add_u32 s8, s88, s8
	s_addc_u32 s9, s89, s9
	s_lshl_b64 s[14:15], s[12:13], 23
	v_readlane_b32 s12, v253, 29
	v_readlane_b32 s13, v253, 30
	s_add_u32 s12, s12, s14
	v_and_b32_e32 v28, 63, v3
	s_addc_u32 s13, s13, s15
	v_readlane_b32 s16, v253, 27
	v_lshlrev_b32_e32 v144, 3, v28
	v_readlane_b32 s17, v253, 28
	s_add_u32 s14, s16, s14
	v_lshl_add_u64 v[6:7], s[12:13], 0, v[144:145]
	s_addc_u32 s15, s17, s15
	v_lshl_add_u64 v[4:5], s[14:15], 0, v[144:145]
	s_load_dwordx2 s[10:11], s[10:11], 0xf0
	v_lshlrev_b32_e32 v144, 5, v28
	v_and_b32_e32 v1, 32, v3
	v_cmp_eq_u32_e64 s[40:41], 0, v1
	v_and_b32_e32 v1, 16, v3
	v_and_b32_e32 v93, 60, v3
	v_cmp_eq_u32_e64 s[42:43], 0, v1
	v_and_b32_e32 v1, 8, v3
	v_cmp_eq_u32_e64 s[44:45], 0, v1
	v_and_b32_e32 v1, 4, v3
	v_or_b32_e32 v34, v34, v93
	v_cmp_eq_u32_e64 s[46:47], 0, v1
	s_waitcnt vmcnt(0)
	v_readlane_b32 s12, v92, 0
	s_ashr_i32 s13, s12, 31
	s_lshl_b64 s[12:13], s[12:13], 9
	v_lshl_add_u64 v[8:9], v[4:5], 0, s[12:13]
	v_lshl_add_u64 v[10:11], v[6:7], 0, s[12:13]
	v_readlane_b32 s12, v92, 1
	s_ashr_i32 s13, s12, 31
	s_lshl_b64 s[12:13], s[12:13], 9
	v_lshl_add_u64 v[12:13], v[6:7], 0, s[12:13]
	global_load_dwordx2 v[8:9], v[8:9], off
	s_nop 0
	global_load_dwordx2 v[82:83], v[10:11], off
	global_load_dwordx2 v[80:81], v[12:13], off
	v_lshl_add_u64 v[10:11], v[4:5], 0, s[12:13]
	v_readlane_b32 s12, v92, 2
	s_ashr_i32 s13, s12, 31
	s_lshl_b64 s[12:13], s[12:13], 9
	v_lshl_add_u64 v[12:13], v[4:5], 0, s[12:13]
	v_lshl_add_u64 v[14:15], v[6:7], 0, s[12:13]
	v_readlane_b32 s12, v92, 3
	s_ashr_i32 s13, s12, 31
	s_lshl_b64 s[12:13], s[12:13], 9
	v_lshl_add_u64 v[16:17], v[6:7], 0, s[12:13]
	global_load_dwordx2 v[10:11], v[10:11], off
	s_nop 0
	global_load_dwordx2 v[12:13], v[12:13], off
	s_nop 0
	global_load_dwordx2 v[78:79], v[14:15], off
	global_load_dwordx2 v[76:77], v[16:17], off
	v_lshl_add_u64 v[14:15], v[4:5], 0, s[12:13]
	v_readlane_b32 s12, v92, 4
	s_ashr_i32 s13, s12, 31
	s_lshl_b64 s[12:13], s[12:13], 9
	v_lshl_add_u64 v[16:17], v[4:5], 0, s[12:13]
	v_lshl_add_u64 v[18:19], v[6:7], 0, s[12:13]
	v_readlane_b32 s12, v92, 5
	s_ashr_i32 s13, s12, 31
	s_lshl_b64 s[12:13], s[12:13], 9
	v_lshl_add_u64 v[20:21], v[6:7], 0, s[12:13]
	global_load_dwordx2 v[14:15], v[14:15], off
	s_nop 0
	global_load_dwordx2 v[16:17], v[16:17], off
	s_nop 0
	global_load_dwordx2 v[74:75], v[18:19], off
	global_load_dwordx2 v[70:71], v[20:21], off
	v_lshl_add_u64 v[18:19], v[4:5], 0, s[12:13]
	v_readlane_b32 s12, v92, 6
	s_ashr_i32 s13, s12, 31
	s_lshl_b64 s[12:13], s[12:13], 9
	v_lshl_add_u64 v[20:21], v[4:5], 0, s[12:13]
	v_lshl_add_u64 v[22:23], v[6:7], 0, s[12:13]
	v_readlane_b32 s12, v92, 7
	s_ashr_i32 s13, s12, 31
	s_lshl_b64 s[12:13], s[12:13], 9
	v_lshl_add_u64 v[24:25], v[6:7], 0, s[12:13]
	global_load_dwordx2 v[18:19], v[18:19], off
	s_nop 0
	global_load_dwordx2 v[20:21], v[20:21], off
	s_nop 0
	global_load_dwordx2 v[68:69], v[22:23], off
	global_load_dwordx2 v[64:65], v[24:25], off
	v_lshl_add_u64 v[22:23], v[4:5], 0, s[12:13]
	v_readlane_b32 s12, v92, 8
	s_ashr_i32 s13, s12, 31
	s_lshl_b64 s[12:13], s[12:13], 9
	v_lshl_add_u64 v[24:25], v[4:5], 0, s[12:13]
	v_lshl_add_u64 v[26:27], v[6:7], 0, s[12:13]
	v_readlane_b32 s12, v92, 9
	s_ashr_i32 s13, s12, 31
	s_lshl_b64 s[12:13], s[12:13], 9
	global_load_dwordx2 v[22:23], v[22:23], off
	s_nop 0
	global_load_dwordx2 v[24:25], v[24:25], off
	s_nop 0
	global_load_dwordx2 v[62:63], v[26:27], off
	v_lshl_add_u64 v[26:27], v[4:5], 0, s[12:13]
	global_load_dwordx2 v[38:39], v[26:27], off
	v_lshl_add_u64 v[26:27], v[6:7], 0, s[12:13]
	v_readlane_b32 s12, v92, 10
	s_ashr_i32 s13, s12, 31
	s_lshl_b64 s[12:13], s[12:13], 9
	global_load_dwordx2 v[66:67], v[26:27], off
	v_lshl_add_u64 v[26:27], v[4:5], 0, s[12:13]
	global_load_dwordx2 v[50:51], v[26:27], off
	v_lshl_add_u64 v[26:27], v[6:7], 0, s[12:13]
	v_readlane_b32 s12, v92, 11
	s_ashr_i32 s13, s12, 31
	s_lshl_b64 s[12:13], s[12:13], 9
	global_load_dwordx2 v[60:61], v[26:27], off
	v_lshl_add_u64 v[26:27], v[4:5], 0, s[12:13]
	global_load_dwordx2 v[48:49], v[26:27], off
	v_lshl_add_u64 v[26:27], v[6:7], 0, s[12:13]
	v_readlane_b32 s12, v92, 12
	s_ashr_i32 s13, s12, 31
	s_lshl_b64 s[12:13], s[12:13], 9
	global_load_dwordx2 v[58:59], v[26:27], off
	v_lshl_add_u64 v[26:27], v[4:5], 0, s[12:13]
	global_load_dwordx2 v[46:47], v[26:27], off
	v_lshl_add_u64 v[26:27], v[6:7], 0, s[12:13]
	v_readlane_b32 s12, v92, 13
	s_ashr_i32 s13, s12, 31
	s_lshl_b64 s[12:13], s[12:13], 9
	global_load_dwordx2 v[56:57], v[26:27], off
	v_lshl_add_u64 v[26:27], v[4:5], 0, s[12:13]
	global_load_dwordx2 v[44:45], v[26:27], off
	v_lshl_add_u64 v[26:27], v[6:7], 0, s[12:13]
	v_readlane_b32 s12, v92, 14
	s_ashr_i32 s13, s12, 31
	s_lshl_b64 s[12:13], s[12:13], 9
	global_load_dwordx2 v[54:55], v[26:27], off
	v_lshl_add_u64 v[26:27], v[4:5], 0, s[12:13]
	global_load_dwordx2 v[42:43], v[26:27], off
	v_lshl_add_u64 v[26:27], v[6:7], 0, s[12:13]
	v_readlane_b32 s12, v92, 15
	s_ashr_i32 s13, s12, 31
	s_lshl_b64 s[12:13], s[12:13], 9
	global_load_dwordx2 v[52:53], v[26:27], off
	v_lshl_add_u64 v[26:27], v[4:5], 0, s[12:13]
	global_load_dwordx2 v[40:41], v[26:27], off
	v_lshl_add_u64 v[26:27], v[6:7], 0, s[12:13]
	global_load_dwordx2 v[36:37], v[26:27], off
	v_readlane_b32 s12, v253, 15
	v_readlane_b32 s13, v253, 16
	s_nop 1
	v_lshl_add_u64 v[26:27], s[12:13], 0, v[144:145]
	v_readlane_b32 s12, v253, 13
	v_lshlrev_b32_e32 v144, 6, v28
	v_readlane_b32 s13, v253, 14
	s_waitcnt lgkmcnt(0)
	v_lshl_add_u64 v[30:31], s[10:11], 0, v[144:145]
	v_readlane_b32 s10, v253, 23
	v_lshl_add_u64 v[28:29], s[12:13], 0, v[144:145]
	v_readlane_b32 s12, v253, 2
	v_readlane_b32 s13, v253, 3
	v_readlane_b32 s11, v253, 24
	v_readlane_b32 s14, v253, 4
	v_lshl_add_u64 v[32:33], s[12:13], 0, v[144:145]
	v_lshl_add_u64 v[34:35], s[10:11], 0, v[34:35]
	s_mov_b64 s[10:11], 0
	v_lshlrev_b32_e32 v144, 2, v2
	v_readlane_b32 s15, v253, 5
	global_load_dwordx4 v[124:127], v[30:31], off
	global_load_dwordx4 v[128:131], v[30:31], off offset:16
	global_load_dwordx4 v[132:135], v[30:31], off offset:32
	global_load_dwordx4 v[136:139], v[30:31], off offset:48
	v_readfirstlane_b32 s62, v4
	v_readfirstlane_b32 s63, v5
	v_readfirstlane_b32 s64, v6
	v_readfirstlane_b32 s65, v7
	v_and_b32_e32 v121, 63, v175
	v_lshlrev_b32_e32 v121, 3, v121

.LBB0_763:
	s_cmpk_ge_i32 s58, 0x70
	s_cselect_b64 s[12:13], -1, 0
	ds_bpermute_b32 v84, v93, v92
	s_and_b64 vcc, s[12:13], s[48:49]
	v_cndmask_b32_e32 v104, v0, v94, vcc
	v_ashrrev_i32_e32 v105, 31, v104
	s_add_i32 s12, s58, 16
	s_and_b32 s12, s12, 0x70
	v_lshlrev_b64 v[104:105], 9, v[104:105]
	v_lshl_add_u64 v[104:105], s[94:95], 0, v[104:105]
	s_lshl_b32 s36, s12, 2
	s_waitcnt lgkmcnt(0)
	s_waitcnt vmcnt(32)
	v_mov_b32_e32 v92, v122
	v_ashrrev_i32_e32 v85, 31, v84
	v_lshl_add_u64 v[104:105], v[104:105], 0, s[36:37]
	v_lshl_add_u64 v[84:85], v[84:85], 3, s[8:9]
	v_lshl_add_u64 v[104:105], v[104:105], 0, v[144:145]
	global_load_dwordx2 v[84:85], v[84:85], off
	s_nop 0
	global_load_dword v86, v[72:73], off
	global_load_dword v122, v[104:105], off
	s_waitcnt vmcnt(19)
	v_dot8_i32_i4 v87, v8, v1, 0
	v_dot8_i32_i4 v104, v8, v88, 0
	v_dot8_i32_i4 v87, v9, v89, v87
	v_dot8_i32_i4 v104, v9, v90, v104
	s_waitcnt vmcnt(19)
	v_dot8_i32_i4 v9, v10, v88, 0
	v_dot8_i32_i4 v9, v11, v90, v9
	v_lshl_add_u32 v87, v87, 4, v104
	v_dot8_i32_i4 v8, v10, v1, 0
	v_dot8_i32_i4 v8, v11, v89, v8
	s_add_i32 s58, s58, 16
	v_lshl_add_u64 v[72:73], v[72:73], 0, 64
	s_nop 0
	v_lshl_add_u32 v104, v8, 4, v9
	v_dot8_i32_i4 v8, v12, v1, 0
	v_dot8_i32_i4 v9, v12, v88, 0
	v_dot8_i32_i4 v8, v13, v89, v8
	v_dot8_i32_i4 v9, v13, v90, v9
	v_readlane_b32 s12, v92, 0
	v_readlane_b32 s28, v92, 8
	v_readlane_b32 s30, v92, 9
	v_lshl_add_u32 v105, v8, 4, v9
	v_dot8_i32_i4 v8, v14, v1, 0
	v_dot8_i32_i4 v9, v14, v88, 0
	v_dot8_i32_i4 v8, v15, v89, v8
	v_dot8_i32_i4 v9, v15, v90, v9
	s_ashr_i32 s13, s12, 31
	v_readlane_b32 s14, v92, 1
	s_ashr_i32 s29, s28, 31
	v_lshl_add_u32 v106, v8, 4, v9
	v_dot8_i32_i4 v8, v16, v1, 0
	v_dot8_i32_i4 v9, v16, v88, 0
	v_dot8_i32_i4 v8, v17, v89, v8
	v_dot8_i32_i4 v9, v17, v90, v9
	s_ashr_i32 s31, s30, 31
	v_readlane_b32 s34, v92, 10
	s_lshl_b64 s[12:13], s[12:13], 9
	v_lshl_add_u32 v107, v8, 4, v9
	v_dot8_i32_i4 v8, v18, v1, 0
	v_dot8_i32_i4 v9, v18, v88, 0
	v_dot8_i32_i4 v8, v19, v89, v8
	v_dot8_i32_i4 v9, v19, v90, v9
	s_ashr_i32 s15, s14, 31
	v_readlane_b32 s16, v92, 2
	s_lshl_b64 s[28:29], s[28:29], 9
	v_lshl_add_u32 v108, v8, 4, v9
	v_dot8_i32_i4 v8, v20, v1, 0
	v_dot8_i32_i4 v9, v20, v88, 0
	v_dot8_i32_i4 v8, v21, v89, v8
	v_dot8_i32_i4 v9, v21, v90, v9
	s_lshl_b64 s[30:31], s[30:31], 9
	s_ashr_i32 s35, s34, 31
	v_readlane_b32 s38, v92, 11
	v_lshl_add_u32 v109, v8, 4, v9
	v_dot8_i32_i4 v8, v22, v1, 0
	v_dot8_i32_i4 v9, v22, v88, 0
	v_dot8_i32_i4 v8, v23, v89, v8
	v_dot8_i32_i4 v9, v23, v90, v9
	s_lshl_b64 s[14:15], s[14:15], 9
	s_ashr_i32 s17, s16, 31
	v_readlane_b32 s18, v92, 3
	v_lshl_add_u32 v110, v8, 4, v9
	v_dot8_i32_i4 v8, v24, v1, 0
	v_dot8_i32_i4 v9, v24, v88, 0
	v_dot8_i32_i4 v8, v25, v89, v8
	v_dot8_i32_i4 v9, v25, v90, v9
	s_lshl_b64 s[34:35], s[34:35], 9
	s_ashr_i32 s39, s38, 31
	s_nop 0
	v_lshl_add_u32 v111, v8, 4, v9
	v_dot8_i32_i4 v8, v38, v1, 0
	v_dot8_i32_i4 v9, v38, v88, 0
	v_dot8_i32_i4 v8, v39, v89, v8
	v_dot8_i32_i4 v9, v39, v90, v9
	s_setprio 2
	v_permlane32_swap_b32 v87, v111
	s_nop 1
	v_lshl_add_u32 v112, v8, 4, v9
	v_dot8_i32_i4 v8, v50, v1, 0
	v_dot8_i32_i4 v9, v50, v88, 0
	v_dot8_i32_i4 v8, v51, v89, v8
	v_dot8_i32_i4 v9, v51, v90, v9
	s_waitcnt lgkmcnt(0)
	v_add_u32_e32 v87, v87, v111
	v_permlane32_swap_b32 v104, v112
	v_lshl_add_u32 v113, v8, 4, v9
	v_dot8_i32_i4 v8, v48, v1, 0
	v_dot8_i32_i4 v9, v48, v88, 0
	v_dot8_i32_i4 v8, v49, v89, v8
	v_dot8_i32_i4 v9, v49, v90, v9
	s_waitcnt lgkmcnt(0)
	v_add_u32_e32 v104, v104, v112
	v_permlane32_swap_b32 v105, v113
	v_lshl_add_u32 v114, v8, 4, v9
	v_dot8_i32_i4 v8, v46, v1, 0
	v_dot8_i32_i4 v9, v46, v88, 0
	v_dot8_i32_i4 v8, v47, v89, v8
	v_dot8_i32_i4 v9, v47, v90, v9
	s_waitcnt lgkmcnt(0)
	v_add_u32_e32 v105, v105, v113
	v_permlane32_swap_b32 v106, v114
	v_lshl_add_u32 v115, v8, 4, v9
	v_dot8_i32_i4 v8, v44, v1, 0
	v_dot8_i32_i4 v9, v44, v88, 0
	v_dot8_i32_i4 v8, v45, v89, v8
	v_dot8_i32_i4 v9, v45, v90, v9
	s_waitcnt lgkmcnt(0)
	v_add_u32_e32 v106, v106, v114
	v_permlane32_swap_b32 v107, v115
	v_lshl_add_u32 v116, v8, 4, v9
	v_dot8_i32_i4 v8, v42, v1, 0
	v_dot8_i32_i4 v9, v42, v88, 0
	v_dot8_i32_i4 v8, v43, v89, v8
	v_dot8_i32_i4 v9, v43, v90, v9
	s_waitcnt lgkmcnt(0)
	v_add_u32_e32 v107, v107, v115
	v_permlane32_swap_b32 v108, v116
	v_lshl_add_u32 v117, v8, 4, v9
	v_dot8_i32_i4 v8, v40, v1, 0
	v_dot8_i32_i4 v9, v40, v88, 0
	v_dot8_i32_i4 v8, v41, v89, v8
	v_dot8_i32_i4 v9, v41, v90, v9
	s_waitcnt lgkmcnt(0)
	v_add_u32_e32 v108, v108, v116
	v_permlane32_swap_b32 v109, v117
	v_lshl_add_u32 v118, v8, 4, v9
	s_waitcnt lgkmcnt(0)
	v_add_u32_e32 v109, v109, v117
	v_permlane32_swap_b32 v110, v118
	v_readlane_b32 s50, v92, 12
	s_lshl_b64 s[16:17], s[16:17], 9
	s_ashr_i32 s19, s18, 31
	s_waitcnt lgkmcnt(0)
	v_add_u32_e32 v110, v110, v118
	v_permlane16_swap_b32 v87, v107
	v_readlane_b32 s20, v92, 4
	s_add_u32 s66, s28, s62
	s_addc_u32 s67, s29, s63
	global_load_dwordx2 v[24:25], v121, s[66:67]
	s_add_u32 s66, s30, s62
	s_addc_u32 s67, s31, s63
	global_load_dwordx2 v[38:39], v121, s[66:67]
	s_waitcnt lgkmcnt(0)
	v_add_u32_e32 v87, v87, v107
	v_permlane16_swap_b32 v104, v108
	s_lshl_b64 s[38:39], s[38:39], 9
	s_ashr_i32 s51, s50, 31
	v_readlane_b32 s52, v92, 13
	s_waitcnt lgkmcnt(0)
	v_add_u32_e32 v104, v104, v108
	v_permlane16_swap_b32 v105, v109
	s_lshl_b64 s[18:19], s[18:19], 9
	s_ashr_i32 s21, s20, 31
	v_readlane_b32 s22, v92, 5
	s_waitcnt lgkmcnt(0)
	v_add_u32_e32 v105, v105, v109
	v_permlane16_swap_b32 v106, v110
	s_add_u32 s66, s34, s62
	s_addc_u32 s67, s35, s63
	global_load_dwordx2 v[50:51], v121, s[66:67]
	s_lshl_b64 s[50:51], s[50:51], 9
	s_ashr_i32 s53, s52, 31
	s_waitcnt lgkmcnt(0)
	v_add_u32_e32 v106, v106, v110
	v_cndmask_b32_e64 v107, v87, v105, s[44:45]
	v_cndmask_b32_e64 v87, v105, v87, s[44:45]
	s_nop 0
	v_readlane_b32 s54, v92, 14
	s_lshl_b64 s[20:21], s[20:21], 9
	s_ashr_i32 s23, s22, 31
	v_readlane_b32 s24, v92, 6
	s_waitcnt lgkmcnt(0)
	v_add_u32_dpp v87, v107, v87 row_ror:8 row_mask:0xf bank_mask:0xf
	v_cndmask_b32_e64 v105, v104, v106, s[44:45]
	s_nop 1
	v_cndmask_b32_e64 v104, v106, v104, s[44:45]
	s_lshl_b64 s[52:53], s[52:53], 9
	s_ashr_i32 s55, s54, 31
	v_readlane_b32 s56, v92, 15
	s_waitcnt lgkmcnt(0)
	v_add_u32_dpp v104, v105, v104 row_ror:8 row_mask:0xf bank_mask:0xf
	v_cndmask_b32_e64 v105, v87, v104, s[46:47]
	v_cndmask_b32_e64 v87, v104, v87, s[46:47]
	s_nop 0
	v_mov_b32_dpp v104, v105 row_half_mirror row_mask:0xf bank_mask:0xf
	s_nop 1
	s_lshl_b64 s[22:23], s[22:23], 9
	s_ashr_i32 s25, s24, 31
	v_readlane_b32 s26, v92, 7
	s_lshl_b64 s[54:55], s[54:55], 9
	s_waitcnt lgkmcnt(0)
	v_add_u32_dpp v87, v104, v87 quad_perm:[3,2,1,0] row_mask:0xf bank_mask:0xf
	s_nop 1
	s_ashr_i32 s57, s56, 31
	s_lshl_b64 s[24:25], s[24:25], 9
	s_ashr_i32 s27, s26, 31
	s_lshl_b64 s[56:57], s[56:57], 9
	s_waitcnt lgkmcnt(0)
	v_add_u32_dpp v87, v87, v87 quad_perm:[2,3,0,1] row_mask:0xf bank_mask:0xf
	s_nop 1
	s_lshl_b64 s[26:27], s[26:27], 9
	s_add_u32 s66, s38, s62
	s_addc_u32 s67, s39, s63
	global_load_dwordx2 v[48:49], v121, s[66:67]
	s_add_u32 s66, s50, s62
	s_addc_u32 s67, s51, s63
	global_load_dwordx2 v[46:47], v121, s[66:67]
	s_add_u32 s66, s52, s62
	s_addc_u32 s67, s53, s63
	global_load_dwordx2 v[44:45], v121, s[66:67]
	s_add_u32 s66, s54, s62
	s_addc_u32 s67, s55, s63
	global_load_dwordx2 v[42:43], v121, s[66:67]
	s_add_u32 s66, s56, s62
	s_addc_u32 s67, s57, s63
	global_load_dwordx2 v[40:41], v121, s[66:67]
	s_add_u32 s66, s12, s62
	s_addc_u32 s67, s13, s63
	global_load_dwordx2 v[8:9], v121, s[66:67]
	s_add_u32 s66, s14, s62
	s_addc_u32 s67, s15, s63
	global_load_dwordx2 v[10:11], v121, s[66:67]
	s_add_u32 s66, s16, s62
	s_addc_u32 s67, s17, s63
	global_load_dwordx2 v[12:13], v121, s[66:67]
	s_add_u32 s66, s18, s62
	s_addc_u32 s67, s19, s63
	global_load_dwordx2 v[14:15], v121, s[66:67]
	s_add_u32 s66, s20, s62
	s_addc_u32 s67, s21, s63
	global_load_dwordx2 v[16:17], v121, s[66:67]
	s_add_u32 s66, s22, s62
	s_addc_u32 s67, s23, s63
	global_load_dwordx2 v[18:19], v121, s[66:67]
	s_add_u32 s66, s24, s62
	s_addc_u32 s67, s25, s63
	global_load_dwordx2 v[20:21], v121, s[66:67]
	s_add_u32 s66, s26, s62
	s_addc_u32 s67, s27, s63
	global_load_dwordx2 v[22:23], v121, s[66:67]
	s_waitcnt lgkmcnt(0)
	v_add_u32_dpp v87, v87, v87 quad_perm:[1,0,3,2] row_mask:0xf bank_mask:0xf
	s_waitcnt vmcnt(17)
	v_mul_f32_e32 v85, v91, v85
	v_cvt_f32_i32_e32 v87, v87
	v_add_f32_e32 v87, v95, v87
	v_mul_f32_e32 v85, v85, v87
	v_mul_f32_e32 v87, 0x3d372713, v85
	v_mul_f32_e32 v87, v85, v87
	v_fma_f32 v87, v85, v87, v85
	v_mul_f32_e32 v87, 0x3fcc422a, v87
	v_mul_f32_e32 v87, 0xbfb8aa3b, v87
	v_exp_f32_e32 v87, v87
	s_nop 0
	v_add_f32_e32 v87, 1.0, v87
	v_rcp_f32_e32 v87, v87
	s_nop 0
	v_pk_mul_f32 v[84:85], v[84:85], v[86:87]
	v_alignbit_b32 v224, v82, v82, 4
	v_pk_mul_f32 v[84:85], v[84:85], v[84:85] op_sel:[0,1] op_sel_hi:[1,0]
	v_cvt_f16_f32_e32 v120, v84
	s_setprio 0
	v_and_b32_e32 v86, 0x7070707, v82
	v_readlane_b32 s36, v120, 0
	v_and_b32_e32 v87, 0x7070707, v224
	v_perm_b32 v86, s2, v205, v86
	v_perm_b32 v87, s2, v205, v87
	v_and_or_b32 v86, v82, s4, v86
	v_and_or_b32 v82, v224, s4, v87
	v_perm_b32 v87, v82, v86, s5
	v_perm_b32 v104, v82, v86, s33
	v_perm_b32 v105, v82, v86, s0
	v_perm_b32 v82, v82, v86, s1
	v_pk_fma_f16 v86, v87, s36, v103 op_sel_hi:[1,0,1]
	v_pk_fma_f16 v87, v104, s36, v102 op_sel_hi:[1,0,1]
	v_alignbit_b32 v225, v83, v83, 4
	v_pk_fma_f16 v82, v82, s36, v100 op_sel_hi:[1,0,1]
	v_and_b32_e32 v100, 0x7070707, v83
	v_and_b32_e32 v102, 0x7070707, v225
	v_perm_b32 v100, s2, v205, v100
	v_perm_b32 v102, s2, v205, v102
	v_and_or_b32 v100, v83, s4, v100
	v_and_or_b32 v83, v225, s4, v102
	v_perm_b32 v102, v83, v100, s5
	v_perm_b32 v103, v83, v100, s33
	v_perm_b32 v104, v83, v100, s0
	v_perm_b32 v83, v83, v100, s1
	v_readlane_b32 s59, v120, 4
	v_alignbit_b32 v224, v80, v80, 4
	v_pk_fma_f16 v101, v105, s36, v101 op_sel_hi:[1,0,1]
	v_pk_fma_f16 v99, v102, s36, v99 op_sel_hi:[1,0,1]
	v_pk_fma_f16 v98, v103, s36, v98 op_sel_hi:[1,0,1]
	v_pk_fma_f16 v97, v104, s36, v97 op_sel_hi:[1,0,1]
	v_pk_fma_f16 v83, v83, s36, v96 op_sel_hi:[1,0,1]
	v_and_b32_e32 v96, 0x7070707, v80
	v_and_b32_e32 v100, 0x7070707, v224
	v_perm_b32 v96, s2, v205, v96
	v_perm_b32 v100, s2, v205, v100
	v_and_or_b32 v96, v80, s4, v96
	v_and_or_b32 v80, v224, s4, v100
	v_perm_b32 v100, v80, v96, s5
	v_perm_b32 v102, v80, v96, s33
	v_perm_b32 v103, v80, v96, s0
	v_perm_b32 v80, v80, v96, s1
	v_pk_fma_f16 v86, v100, s59, v86 op_sel_hi:[1,0,1]
	v_alignbit_b32 v225, v81, v81, 4
	v_pk_fma_f16 v80, v80, s59, v82 op_sel_hi:[1,0,1]
	v_and_b32_e32 v82, 0x7070707, v81
	v_and_b32_e32 v100, 0x7070707, v225
	v_pk_fma_f16 v96, v103, s59, v101 op_sel_hi:[1,0,1]
	v_perm_b32 v82, s2, v205, v82
	v_perm_b32 v100, s2, v205, v100
	v_and_or_b32 v82, v81, s4, v82
	v_and_or_b32 v81, v225, s4, v100
	v_perm_b32 v100, v81, v82, s5
	v_pk_fma_f16 v87, v102, s59, v87 op_sel_hi:[1,0,1]
	v_perm_b32 v101, v81, v82, s33
	v_perm_b32 v102, v81, v82, s0
	v_perm_b32 v81, v81, v82, s1
	v_pk_fma_f16 v82, v100, s59, v99 op_sel_hi:[1,0,1]
	v_readlane_b32 s60, v120, 8
	v_alignbit_b32 v224, v78, v78, 4
	v_pk_fma_f16 v98, v101, s59, v98 op_sel_hi:[1,0,1]
	v_pk_fma_f16 v97, v102, s59, v97 op_sel_hi:[1,0,1]
	v_pk_fma_f16 v81, v81, s59, v83 op_sel_hi:[1,0,1]
	v_and_b32_e32 v85, 0x7070707, v78
	v_and_b32_e32 v99, 0x7070707, v224
	v_perm_b32 v85, s2, v205, v85
	v_perm_b32 v99, s2, v205, v99
	v_and_or_b32 v85, v78, s4, v85
	v_and_or_b32 v78, v224, s4, v99
	v_perm_b32 v99, v78, v85, s5
	v_perm_b32 v100, v78, v85, s33
	v_perm_b32 v101, v78, v85, s0
	v_perm_b32 v78, v78, v85, s1
	v_pk_fma_f16 v85, v99, s60, v86 op_sel_hi:[1,0,1]
	v_pk_fma_f16 v86, v100, s60, v87 op_sel_hi:[1,0,1]
	v_pk_fma_f16 v87, v101, s60, v96 op_sel_hi:[1,0,1]
	v_alignbit_b32 v225, v79, v79, 4
	v_pk_fma_f16 v78, v78, s60, v80 op_sel_hi:[1,0,1]
	v_and_b32_e32 v80, 0x7070707, v79
	v_and_b32_e32 v96, 0x7070707, v225
	v_perm_b32 v80, s2, v205, v80
	v_perm_b32 v96, s2, v205, v96
	v_and_or_b32 v80, v79, s4, v80
	v_and_or_b32 v79, v225, s4, v96
	v_perm_b32 v96, v79, v80, s5
	v_perm_b32 v100, v79, v80, s0
	v_perm_b32 v99, v79, v80, s33
	v_perm_b32 v79, v79, v80, s1
	v_pk_fma_f16 v80, v96, s60, v82 op_sel_hi:[1,0,1]
	v_pk_fma_f16 v96, v100, s60, v97 op_sel_hi:[1,0,1]
	v_readlane_b32 s36, v120, 12
	v_alignbit_b32 v224, v76, v76, 4
	v_pk_fma_f16 v82, v99, s60, v98 op_sel_hi:[1,0,1]
	v_pk_fma_f16 v79, v79, s60, v81 op_sel_hi:[1,0,1]
	v_and_b32_e32 v83, 0x7070707, v76
	v_and_b32_e32 v97, 0x7070707, v224
	v_perm_b32 v83, s2, v205, v83
	v_perm_b32 v97, s2, v205, v97
	v_and_or_b32 v83, v76, s4, v83
	v_and_or_b32 v76, v224, s4, v97
	v_perm_b32 v97, v76, v83, s5
	v_perm_b32 v98, v76, v83, s33
	v_perm_b32 v99, v76, v83, s0
	v_perm_b32 v76, v76, v83, s1
	v_pk_fma_f16 v83, v97, s36, v85 op_sel_hi:[1,0,1]
	v_pk_fma_f16 v85, v98, s36, v86 op_sel_hi:[1,0,1]
	v_pk_fma_f16 v86, v99, s36, v87 op_sel_hi:[1,0,1]
	v_alignbit_b32 v225, v77, v77, 4
	v_pk_fma_f16 v76, v76, s36, v78 op_sel_hi:[1,0,1]
	v_and_b32_e32 v78, 0x7070707, v77
	v_and_b32_e32 v87, 0x7070707, v225
	v_perm_b32 v78, s2, v205, v78
	v_perm_b32 v87, s2, v205, v87
	v_and_or_b32 v78, v77, s4, v78
	v_and_or_b32 v77, v225, s4, v87
	v_perm_b32 v87, v77, v78, s5
	v_perm_b32 v97, v77, v78, s33
	v_perm_b32 v98, v77, v78, s0
	v_perm_b32 v77, v77, v78, s1
	v_pk_fma_f16 v78, v87, s36, v80 op_sel_hi:[1,0,1]
	v_readlane_b32 s59, v120, 16
	v_alignbit_b32 v224, v74, v74, 4
	v_pk_fma_f16 v80, v97, s36, v82 op_sel_hi:[1,0,1]
	v_pk_fma_f16 v82, v98, s36, v96 op_sel_hi:[1,0,1]
	v_pk_fma_f16 v77, v77, s36, v79 op_sel_hi:[1,0,1]
	v_and_b32_e32 v81, 0x7070707, v74
	v_and_b32_e32 v87, 0x7070707, v224
	v_perm_b32 v81, s2, v205, v81
	v_perm_b32 v87, s2, v205, v87
	v_and_or_b32 v81, v74, s4, v81
	v_and_or_b32 v74, v224, s4, v87
	v_perm_b32 v87, v74, v81, s5
	v_perm_b32 v96, v74, v81, s33
	v_perm_b32 v97, v74, v81, s0
	v_perm_b32 v74, v74, v81, s1
	v_pk_fma_f16 v81, v87, s59, v83 op_sel_hi:[1,0,1]
	v_pk_fma_f16 v83, v96, s59, v85 op_sel_hi:[1,0,1]
	v_pk_fma_f16 v85, v97, s59, v86 op_sel_hi:[1,0,1]
	v_alignbit_b32 v225, v75, v75, 4
	v_pk_fma_f16 v74, v74, s59, v76 op_sel_hi:[1,0,1]
	v_and_b32_e32 v76, 0x7070707, v75
	v_and_b32_e32 v86, 0x7070707, v225
	v_perm_b32 v76, s2, v205, v76
	v_perm_b32 v86, s2, v205, v86
	v_and_or_b32 v76, v75, s4, v76
	v_and_or_b32 v75, v225, s4, v86
	v_perm_b32 v86, v75, v76, s5
	v_perm_b32 v87, v75, v76, s33
	v_perm_b32 v96, v75, v76, s0
	v_perm_b32 v75, v75, v76, s1
	v_pk_fma_f16 v76, v86, s59, v78 op_sel_hi:[1,0,1]
	v_pk_fma_f16 v78, v87, s59, v80 op_sel_hi:[1,0,1]
	v_pk_fma_f16 v80, v96, s59, v82 op_sel_hi:[1,0,1]
	v_readlane_b32 s60, v120, 20
	v_alignbit_b32 v224, v70, v70, 4
	v_pk_fma_f16 v75, v75, s59, v77 op_sel_hi:[1,0,1]
	v_and_b32_e32 v79, 0x7070707, v70
	v_and_b32_e32 v82, 0x7070707, v224
	v_perm_b32 v79, s2, v205, v79
	v_perm_b32 v82, s2, v205, v82
	v_and_or_b32 v79, v70, s4, v79
	v_and_or_b32 v70, v224, s4, v82
	v_perm_b32 v82, v70, v79, s5
	v_perm_b32 v86, v70, v79, s33
	v_perm_b32 v87, v70, v79, s0
	v_perm_b32 v70, v70, v79, s1
	v_pk_fma_f16 v79, v82, s60, v81 op_sel_hi:[1,0,1]
	v_pk_fma_f16 v81, v86, s60, v83 op_sel_hi:[1,0,1]
	v_alignbit_b32 v225, v71, v71, 4
	v_pk_fma_f16 v70, v70, s60, v74 op_sel_hi:[1,0,1]
	v_and_b32_e32 v74, 0x7070707, v71
	v_and_b32_e32 v83, 0x7070707, v225
	v_pk_fma_f16 v82, v87, s60, v85 op_sel_hi:[1,0,1]
	v_perm_b32 v74, s2, v205, v74
	v_perm_b32 v83, s2, v205, v83
	v_and_or_b32 v74, v71, s4, v74
	v_and_or_b32 v71, v225, s4, v83
	v_perm_b32 v83, v71, v74, s5
	v_perm_b32 v85, v71, v74, s33
	v_perm_b32 v86, v71, v74, s0
	v_perm_b32 v71, v71, v74, s1
	v_pk_fma_f16 v74, v83, s60, v76 op_sel_hi:[1,0,1]
	v_pk_fma_f16 v76, v85, s60, v78 op_sel_hi:[1,0,1]
	v_pk_fma_f16 v78, v86, s60, v80 op_sel_hi:[1,0,1]
	v_readlane_b32 s36, v120, 24
	v_alignbit_b32 v224, v68, v68, 4
	v_pk_fma_f16 v71, v71, s60, v75 op_sel_hi:[1,0,1]
	v_and_b32_e32 v77, 0x7070707, v68
	v_and_b32_e32 v80, 0x7070707, v224
	v_perm_b32 v77, s2, v205, v77
	v_perm_b32 v80, s2, v205, v80
	v_and_or_b32 v77, v68, s4, v77
	v_and_or_b32 v68, v224, s4, v80
	v_perm_b32 v80, v68, v77, s5
	v_perm_b32 v83, v68, v77, s33
	v_perm_b32 v85, v68, v77, s0
	v_perm_b32 v68, v68, v77, s1
	v_pk_fma_f16 v77, v80, s36, v79 op_sel_hi:[1,0,1]
	v_pk_fma_f16 v79, v83, s36, v81 op_sel_hi:[1,0,1]
	v_alignbit_b32 v225, v69, v69, 4
	v_pk_fma_f16 v68, v68, s36, v70 op_sel_hi:[1,0,1]
	v_and_b32_e32 v70, 0x7070707, v69
	v_and_b32_e32 v81, 0x7070707, v225
	v_pk_fma_f16 v80, v85, s36, v82 op_sel_hi:[1,0,1]
	v_perm_b32 v70, s2, v205, v70
	v_perm_b32 v81, s2, v205, v81
	v_and_or_b32 v70, v69, s4, v70
	v_and_or_b32 v69, v225, s4, v81
	v_perm_b32 v81, v69, v70, s5
	v_perm_b32 v82, v69, v70, s33
	v_perm_b32 v83, v69, v70, s0
	v_perm_b32 v69, v69, v70, s1
	v_pk_fma_f16 v70, v81, s36, v74 op_sel_hi:[1,0,1]
	v_pk_fma_f16 v74, v82, s36, v76 op_sel_hi:[1,0,1]
	v_pk_fma_f16 v76, v83, s36, v78 op_sel_hi:[1,0,1]
	v_readlane_b32 s59, v120, 28
	v_alignbit_b32 v224, v64, v64, 4
	v_pk_fma_f16 v69, v69, s36, v71 op_sel_hi:[1,0,1]
	v_and_b32_e32 v75, 0x7070707, v64
	v_and_b32_e32 v78, 0x7070707, v224
	v_perm_b32 v75, s2, v205, v75
	v_perm_b32 v78, s2, v205, v78
	v_and_or_b32 v75, v64, s4, v75
	v_and_or_b32 v64, v224, s4, v78
	v_perm_b32 v78, v64, v75, s5
	v_perm_b32 v81, v64, v75, s33
	v_perm_b32 v82, v64, v75, s0
	v_perm_b32 v64, v64, v75, s1
	v_pk_fma_f16 v75, v78, s59, v77 op_sel_hi:[1,0,1]
	v_pk_fma_f16 v77, v81, s59, v79 op_sel_hi:[1,0,1]
	v_alignbit_b32 v225, v65, v65, 4
	v_pk_fma_f16 v64, v64, s59, v68 op_sel_hi:[1,0,1]
	v_and_b32_e32 v68, 0x7070707, v65
	v_and_b32_e32 v79, 0x7070707, v225
	v_pk_fma_f16 v78, v82, s59, v80 op_sel_hi:[1,0,1]
	v_perm_b32 v68, s2, v205, v68
	v_perm_b32 v79, s2, v205, v79
	v_and_or_b32 v68, v65, s4, v68
	v_and_or_b32 v65, v225, s4, v79
	v_perm_b32 v79, v65, v68, s5
	v_perm_b32 v80, v65, v68, s33
	v_perm_b32 v81, v65, v68, s0
	v_perm_b32 v65, v65, v68, s1
	v_pk_fma_f16 v68, v79, s59, v70 op_sel_hi:[1,0,1]
	v_pk_fma_f16 v70, v80, s59, v74 op_sel_hi:[1,0,1]
	v_pk_fma_f16 v74, v81, s59, v76 op_sel_hi:[1,0,1]
	v_readlane_b32 s60, v120, 32
	v_alignbit_b32 v224, v62, v62, 4
	v_pk_fma_f16 v65, v65, s59, v69 op_sel_hi:[1,0,1]
	v_and_b32_e32 v71, 0x7070707, v62
	v_and_b32_e32 v76, 0x7070707, v224
	v_perm_b32 v71, s2, v205, v71
	v_perm_b32 v76, s2, v205, v76
	v_and_or_b32 v71, v62, s4, v71
	v_and_or_b32 v62, v224, s4, v76
	v_perm_b32 v76, v62, v71, s5
	v_perm_b32 v79, v62, v71, s33
	v_perm_b32 v80, v62, v71, s0
	v_perm_b32 v62, v62, v71, s1
	v_pk_fma_f16 v71, v76, s60, v75 op_sel_hi:[1,0,1]
	v_pk_fma_f16 v75, v79, s60, v77 op_sel_hi:[1,0,1]
	v_alignbit_b32 v225, v63, v63, 4
	v_pk_fma_f16 v62, v62, s60, v64 op_sel_hi:[1,0,1]
	v_and_b32_e32 v64, 0x7070707, v63
	v_and_b32_e32 v77, 0x7070707, v225
	v_pk_fma_f16 v76, v80, s60, v78 op_sel_hi:[1,0,1]
	v_perm_b32 v64, s2, v205, v64
	v_perm_b32 v77, s2, v205, v77
	v_and_or_b32 v64, v63, s4, v64
	v_and_or_b32 v63, v225, s4, v77
	v_perm_b32 v77, v63, v64, s5
	v_perm_b32 v78, v63, v64, s33
	v_perm_b32 v79, v63, v64, s0
	v_perm_b32 v63, v63, v64, s1
	v_pk_fma_f16 v64, v77, s60, v68 op_sel_hi:[1,0,1]
	v_pk_fma_f16 v68, v78, s60, v70 op_sel_hi:[1,0,1]
	v_pk_fma_f16 v70, v79, s60, v74 op_sel_hi:[1,0,1]
	v_readlane_b32 s36, v120, 36
	v_alignbit_b32 v224, v66, v66, 4
	v_pk_fma_f16 v63, v63, s60, v65 op_sel_hi:[1,0,1]
	v_and_b32_e32 v69, 0x7070707, v66
	v_and_b32_e32 v74, 0x7070707, v224
	v_perm_b32 v69, s2, v205, v69
	v_perm_b32 v74, s2, v205, v74
	v_and_or_b32 v69, v66, s4, v69
	v_and_or_b32 v66, v224, s4, v74
	v_perm_b32 v74, v66, v69, s5
	v_perm_b32 v77, v66, v69, s33
	v_perm_b32 v78, v66, v69, s0
	v_perm_b32 v66, v66, v69, s1
	v_pk_fma_f16 v69, v74, s36, v71 op_sel_hi:[1,0,1]
	v_pk_fma_f16 v71, v77, s36, v75 op_sel_hi:[1,0,1]
	v_alignbit_b32 v225, v67, v67, 4
	v_pk_fma_f16 v62, v66, s36, v62 op_sel_hi:[1,0,1]
	v_and_b32_e32 v66, 0x7070707, v67
	v_and_b32_e32 v75, 0x7070707, v225
	v_pk_fma_f16 v74, v78, s36, v76 op_sel_hi:[1,0,1]
	v_perm_b32 v66, s2, v205, v66
	v_perm_b32 v75, s2, v205, v75
	v_and_or_b32 v66, v67, s4, v66
	v_and_or_b32 v67, v225, s4, v75
	v_perm_b32 v76, v67, v66, s33
	v_perm_b32 v77, v67, v66, s0
	v_perm_b32 v75, v67, v66, s5
	v_perm_b32 v66, v67, v66, s1
	v_pk_fma_f16 v67, v76, s36, v68 op_sel_hi:[1,0,1]
	v_pk_fma_f16 v68, v77, s36, v70 op_sel_hi:[1,0,1]
	v_readlane_b32 s59, v120, 40
	v_alignbit_b32 v224, v60, v60, 4
	v_pk_fma_f16 v64, v75, s36, v64 op_sel_hi:[1,0,1]
	v_pk_fma_f16 v63, v66, s36, v63 op_sel_hi:[1,0,1]
	v_and_b32_e32 v66, 0x7070707, v60
	v_and_b32_e32 v70, 0x7070707, v224
	v_perm_b32 v66, s2, v205, v66
	v_perm_b32 v70, s2, v205, v70
	v_and_or_b32 v66, v60, s4, v66
	v_and_or_b32 v60, v224, s4, v70
	v_perm_b32 v70, v60, v66, s5
	v_perm_b32 v75, v60, v66, s33
	v_perm_b32 v76, v60, v66, s0
	v_perm_b32 v60, v60, v66, s1
	v_pk_fma_f16 v66, v70, s59, v69 op_sel_hi:[1,0,1]
	v_pk_fma_f16 v69, v75, s59, v71 op_sel_hi:[1,0,1]
	v_alignbit_b32 v225, v61, v61, 4
	v_pk_fma_f16 v60, v60, s59, v62 op_sel_hi:[1,0,1]
	v_and_b32_e32 v62, 0x7070707, v61
	v_and_b32_e32 v71, 0x7070707, v225
	v_pk_fma_f16 v70, v76, s59, v74 op_sel_hi:[1,0,1]
	v_perm_b32 v62, s2, v205, v62
	v_perm_b32 v71, s2, v205, v71
	v_and_or_b32 v62, v61, s4, v62
	v_and_or_b32 v61, v225, s4, v71
	v_perm_b32 v71, v61, v62, s5
	v_perm_b32 v74, v61, v62, s33
	v_perm_b32 v75, v61, v62, s0
	v_perm_b32 v61, v61, v62, s1
	v_pk_fma_f16 v62, v71, s59, v64 op_sel_hi:[1,0,1]
	v_pk_fma_f16 v64, v74, s59, v67 op_sel_hi:[1,0,1]
	v_pk_fma_f16 v67, v75, s59, v68 op_sel_hi:[1,0,1]
	v_readlane_b32 s60, v120, 44
	v_alignbit_b32 v224, v58, v58, 4
	v_pk_fma_f16 v61, v61, s59, v63 op_sel_hi:[1,0,1]
	v_and_b32_e32 v65, 0x7070707, v58
	v_and_b32_e32 v68, 0x7070707, v224
	v_perm_b32 v65, s2, v205, v65
	v_perm_b32 v68, s2, v205, v68
	v_and_or_b32 v65, v58, s4, v65
	v_and_or_b32 v58, v224, s4, v68
	v_perm_b32 v68, v58, v65, s5
	v_perm_b32 v71, v58, v65, s33
	v_perm_b32 v74, v58, v65, s0
	v_perm_b32 v58, v58, v65, s1
	v_pk_fma_f16 v65, v68, s60, v66 op_sel_hi:[1,0,1]
	v_pk_fma_f16 v66, v71, s60, v69 op_sel_hi:[1,0,1]
	v_alignbit_b32 v225, v59, v59, 4
	v_pk_fma_f16 v58, v58, s60, v60 op_sel_hi:[1,0,1]
	v_and_b32_e32 v60, 0x7070707, v59
	v_and_b32_e32 v69, 0x7070707, v225
	v_pk_fma_f16 v68, v74, s60, v70 op_sel_hi:[1,0,1]
	v_perm_b32 v60, s2, v205, v60
	v_perm_b32 v69, s2, v205, v69
	v_and_or_b32 v60, v59, s4, v60
	v_and_or_b32 v59, v225, s4, v69
	v_perm_b32 v69, v59, v60, s5
	v_perm_b32 v70, v59, v60, s33
	v_perm_b32 v71, v59, v60, s0
	v_perm_b32 v59, v59, v60, s1
	v_pk_fma_f16 v60, v69, s60, v62 op_sel_hi:[1,0,1]
	v_pk_fma_f16 v62, v70, s60, v64 op_sel_hi:[1,0,1]
	v_pk_fma_f16 v64, v71, s60, v67 op_sel_hi:[1,0,1]
	v_readlane_b32 s36, v120, 48
	v_alignbit_b32 v224, v56, v56, 4
	v_pk_fma_f16 v59, v59, s60, v61 op_sel_hi:[1,0,1]
	v_and_b32_e32 v63, 0x7070707, v56
	v_and_b32_e32 v67, 0x7070707, v224
	v_perm_b32 v63, s2, v205, v63
	v_perm_b32 v67, s2, v205, v67
	v_and_or_b32 v63, v56, s4, v63
	v_and_or_b32 v56, v224, s4, v67
	v_perm_b32 v67, v56, v63, s5
	v_perm_b32 v69, v56, v63, s33
	v_perm_b32 v70, v56, v63, s0
	v_perm_b32 v56, v56, v63, s1
	v_pk_fma_f16 v63, v67, s36, v65 op_sel_hi:[1,0,1]
	v_alignbit_b32 v225, v57, v57, 4
	v_pk_fma_f16 v56, v56, s36, v58 op_sel_hi:[1,0,1]
	v_and_b32_e32 v58, 0x7070707, v57
	v_and_b32_e32 v67, 0x7070707, v225
	v_pk_fma_f16 v65, v69, s36, v66 op_sel_hi:[1,0,1]
	v_pk_fma_f16 v66, v70, s36, v68 op_sel_hi:[1,0,1]
	v_perm_b32 v58, s2, v205, v58
	v_perm_b32 v67, s2, v205, v67
	v_and_or_b32 v58, v57, s4, v58
	v_and_or_b32 v57, v225, s4, v67
	v_perm_b32 v67, v57, v58, s5
	v_perm_b32 v68, v57, v58, s33
	v_perm_b32 v69, v57, v58, s0
	v_perm_b32 v57, v57, v58, s1
	v_pk_fma_f16 v58, v67, s36, v60 op_sel_hi:[1,0,1]
	v_pk_fma_f16 v60, v68, s36, v62 op_sel_hi:[1,0,1]
	v_pk_fma_f16 v62, v69, s36, v64 op_sel_hi:[1,0,1]
	v_readlane_b32 s59, v120, 52
	v_alignbit_b32 v224, v54, v54, 4
	v_pk_fma_f16 v57, v57, s36, v59 op_sel_hi:[1,0,1]
	v_and_b32_e32 v61, 0x7070707, v54
	v_and_b32_e32 v64, 0x7070707, v224
	v_perm_b32 v61, s2, v205, v61
	v_perm_b32 v64, s2, v205, v64
	v_and_or_b32 v61, v54, s4, v61
	v_and_or_b32 v54, v224, s4, v64
	v_perm_b32 v64, v54, v61, s5
	v_perm_b32 v67, v54, v61, s33
	v_perm_b32 v68, v54, v61, s0
	v_perm_b32 v54, v54, v61, s1
	v_pk_fma_f16 v61, v64, s59, v63 op_sel_hi:[1,0,1]
	v_pk_fma_f16 v63, v67, s59, v65 op_sel_hi:[1,0,1]
	v_alignbit_b32 v225, v55, v55, 4
	v_pk_fma_f16 v54, v54, s59, v56 op_sel_hi:[1,0,1]
	v_and_b32_e32 v56, 0x7070707, v55
	v_and_b32_e32 v65, 0x7070707, v225
	v_pk_fma_f16 v64, v68, s59, v66 op_sel_hi:[1,0,1]
	v_perm_b32 v56, s2, v205, v56
	v_perm_b32 v65, s2, v205, v65
	v_and_or_b32 v56, v55, s4, v56
	v_and_or_b32 v55, v225, s4, v65
	v_perm_b32 v65, v55, v56, s5
	v_perm_b32 v66, v55, v56, s33
	v_perm_b32 v67, v55, v56, s0
	v_perm_b32 v55, v55, v56, s1
	v_pk_fma_f16 v56, v65, s59, v58 op_sel_hi:[1,0,1]
	v_pk_fma_f16 v58, v66, s59, v60 op_sel_hi:[1,0,1]
	v_pk_fma_f16 v60, v67, s59, v62 op_sel_hi:[1,0,1]
	v_readlane_b32 s60, v120, 56
	v_alignbit_b32 v224, v52, v52, 4
	v_pk_fma_f16 v55, v55, s59, v57 op_sel_hi:[1,0,1]
	v_and_b32_e32 v59, 0x7070707, v52
	v_and_b32_e32 v62, 0x7070707, v224
	v_perm_b32 v59, s2, v205, v59
	v_perm_b32 v62, s2, v205, v62
	v_and_or_b32 v59, v52, s4, v59
	v_and_or_b32 v52, v224, s4, v62
	v_perm_b32 v62, v52, v59, s5
	v_perm_b32 v65, v52, v59, s33
	v_perm_b32 v66, v52, v59, s0
	v_perm_b32 v52, v52, v59, s1
	v_pk_fma_f16 v59, v62, s60, v61 op_sel_hi:[1,0,1]
	v_pk_fma_f16 v61, v65, s60, v63 op_sel_hi:[1,0,1]
	v_alignbit_b32 v225, v53, v53, 4
	v_pk_fma_f16 v52, v52, s60, v54 op_sel_hi:[1,0,1]
	v_and_b32_e32 v54, 0x7070707, v53
	v_and_b32_e32 v63, 0x7070707, v225
	v_pk_fma_f16 v62, v66, s60, v64 op_sel_hi:[1,0,1]
	v_perm_b32 v54, s2, v205, v54
	v_perm_b32 v63, s2, v205, v63
	v_and_or_b32 v54, v53, s4, v54
	v_and_or_b32 v53, v225, s4, v63
	v_perm_b32 v63, v53, v54, s5
	v_perm_b32 v64, v53, v54, s33
	v_perm_b32 v65, v53, v54, s0
	v_perm_b32 v53, v53, v54, s1
	v_pk_fma_f16 v54, v63, s60, v56 op_sel_hi:[1,0,1]
	v_pk_fma_f16 v56, v64, s60, v58 op_sel_hi:[1,0,1]
	v_pk_fma_f16 v58, v65, s60, v60 op_sel_hi:[1,0,1]
	v_readlane_b32 s36, v120, 60
	v_alignbit_b32 v224, v36, v36, 4
	v_pk_fma_f16 v53, v53, s60, v55 op_sel_hi:[1,0,1]
	v_and_b32_e32 v57, 0x7070707, v36
	v_and_b32_e32 v60, 0x7070707, v224
	v_perm_b32 v57, s2, v205, v57
	v_perm_b32 v60, s2, v205, v60
	v_and_or_b32 v57, v36, s4, v57
	v_and_or_b32 v36, v224, s4, v60
	v_perm_b32 v60, v36, v57, s5
	v_perm_b32 v63, v36, v57, s33
	v_perm_b32 v64, v36, v57, s0
	v_perm_b32 v36, v36, v57, s1
	v_pk_fma_f16 v100, v36, s36, v52 op_sel_hi:[1,0,1]
	v_alignbit_b32 v225, v37, v37, 4
	v_and_b32_e32 v36, 0x7070707, v37
	v_and_b32_e32 v52, 0x7070707, v225
	v_perm_b32 v36, s2, v205, v36
	v_perm_b32 v52, s2, v205, v52
	v_and_or_b32 v36, v37, s4, v36
	v_and_or_b32 v37, v225, s4, v52
	v_pk_fma_f16 v103, v60, s36, v59 op_sel_hi:[1,0,1]
	v_perm_b32 v52, v37, v36, s5
	v_perm_b32 v57, v37, v36, s33
	v_perm_b32 v59, v37, v36, s0
	v_perm_b32 v36, v37, v36, s1
	v_pk_fma_f16 v96, v36, s36, v53 op_sel_hi:[1,0,1]
	s_add_u32 s66, s12, s64
	s_addc_u32 s67, s13, s65
	global_load_dwordx2 v[82:83], v121, s[66:67]
	s_add_u32 s66, s14, s64
	s_addc_u32 s67, s15, s65
	global_load_dwordx2 v[80:81], v121, s[66:67]
	s_add_u32 s66, s16, s64
	s_addc_u32 s67, s17, s65
	global_load_dwordx2 v[78:79], v121, s[66:67]
	s_add_u32 s66, s18, s64
	s_addc_u32 s67, s19, s65
	global_load_dwordx2 v[76:77], v121, s[66:67]
	s_add_u32 s66, s20, s64
	s_addc_u32 s67, s21, s65
	global_load_dwordx2 v[74:75], v121, s[66:67]
	s_add_u32 s66, s22, s64
	s_addc_u32 s67, s23, s65
	global_load_dwordx2 v[70:71], v121, s[66:67]
	v_pk_fma_f16 v101, v64, s36, v62 op_sel_hi:[1,0,1]
	s_add_u32 s66, s24, s64
	s_addc_u32 s67, s25, s65
	global_load_dwordx2 v[68:69], v121, s[66:67]
	s_add_u32 s66, s26, s64
	s_addc_u32 s67, s27, s65
	global_load_dwordx2 v[64:65], v121, s[66:67]
	v_pk_fma_f16 v102, v63, s36, v61 op_sel_hi:[1,0,1]
	s_add_u32 s66, s28, s64
	s_addc_u32 s67, s29, s65
	global_load_dwordx2 v[62:63], v121, s[66:67]
	s_add_u32 s66, s30, s64
	s_addc_u32 s67, s31, s65
	global_load_dwordx2 v[66:67], v121, s[66:67]
	s_add_u32 s66, s34, s64
	s_addc_u32 s67, s35, s65
	global_load_dwordx2 v[60:61], v121, s[66:67]
	v_pk_fma_f16 v97, v59, s36, v58 op_sel_hi:[1,0,1]
	s_add_u32 s66, s38, s64
	s_addc_u32 s67, s39, s65
	global_load_dwordx2 v[58:59], v121, s[66:67]
	v_pk_fma_f16 v98, v57, s36, v56 op_sel_hi:[1,0,1]
	s_add_u32 s66, s50, s64
	s_addc_u32 s67, s51, s65
	global_load_dwordx2 v[56:57], v121, s[66:67]
	v_pk_fma_f16 v99, v52, s36, v54 op_sel_hi:[1,0,1]
	s_add_u32 s66, s52, s64
	s_addc_u32 s67, s53, s65
	global_load_dwordx2 v[54:55], v121, s[66:67]
	s_add_u32 s66, s54, s64
	s_addc_u32 s67, s55, s65
	global_load_dwordx2 v[52:53], v121, s[66:67]
	s_nop 0
	s_nop 0
	s_nop 0
	s_nop 0
	s_nop 0
	s_nop 0
	s_nop 0
	s_add_u32 s66, s56, s64
	s_addc_u32 s67, s57, s65
	global_load_dwordx2 v[36:37], v121, s[66:67]
	s_cmpk_eq_i32 s58, 0x90
	s_cbranch_scc0 .LBB0_763
	v_lshlrev_b64 v[0:1], 2, v[2:3]
	v_lshl_add_u64 v[2:3], v[28:29], 0, v[0:1]
	v_mov_b32_e32 v104, v208
	v_mov_b32_e32 v105, v209
	v_mov_b32_e32 v106, v210
	v_mov_b32_e32 v107, v211
	v_mov_b32_e32 v108, v212
	v_mov_b32_e32 v109, v213
	v_mov_b32_e32 v110, v214
	v_mov_b32_e32 v111, v215
	v_mov_b32_e32 v86, v216
	v_mov_b32_e32 v87, v217
	v_mov_b32_e32 v88, v218
	v_mov_b32_e32 v89, v219
	v_mov_b32_e32 v112, v220
	v_mov_b32_e32 v113, v221
	v_mov_b32_e32 v114, v222
	v_mov_b32_e32 v115, v223
	v_lshl_add_u64 v[72:73], v[32:33], 0, v[0:1]
	v_cvt_f32_f16_sdwa v1, v103 dst_sel:DWORD dst_unused:UNUSED_PAD src0_sel:WORD_1
	v_cvt_f32_f16_e32 v0, v103
	v_cvt_f32_f16_sdwa v91, v102 dst_sel:DWORD dst_unused:UNUSED_PAD src0_sel:WORD_1
	v_cvt_f32_f16_e32 v90, v102
	v_cvt_f32_f16_sdwa v103, v101 dst_sel:DWORD dst_unused:UNUSED_PAD src0_sel:WORD_1
	v_cvt_f32_f16_e32 v102, v101
	v_cvt_f32_f16_sdwa v101, v100 dst_sel:DWORD dst_unused:UNUSED_PAD src0_sel:WORD_1
	v_cvt_f32_f16_e32 v100, v100
	s_mov_b32 s18, 0x800000
	v_readlane_b32 s12, v255, 5
	v_readlane_b32 s13, v255, 6
	v_pk_add_f32 v[86:87], v[86:87], v[102:103]
	v_pk_add_f32 v[84:85], v[112:113], v[0:1]
	v_mov_b32_e32 v102, v85
	v_mov_b32_e32 v103, v87
	v_pk_add_f32 v[90:91], v[114:115], v[90:91]
	v_pk_add_f32 v[88:89], v[88:89], v[100:101]
	v_mov_b32_e32 v100, v84
	v_mov_b32_e32 v101, v86
	v_pk_mul_f32 v[102:103], v[102:103], v[102:103]
	v_mov_b32_e32 v112, v91
	v_pk_fma_f32 v[100:101], v[100:101], v[100:101], v[102:103]
	v_mov_b32_e32 v102, v90
	v_mov_b32_e32 v103, v88
	v_pk_fma_f32 v[100:101], v[102:103], v[102:103], v[100:101]
	v_cvt_f32_f16_sdwa v103, v99 dst_sel:DWORD dst_unused:UNUSED_PAD src0_sel:WORD_1
	v_cvt_f32_f16_e32 v102, v99
	v_cvt_f32_f16_sdwa v99, v98 dst_sel:DWORD dst_unused:UNUSED_PAD src0_sel:WORD_1
	v_cvt_f32_f16_e32 v98, v98
	v_mov_b32_e32 v113, v89
	v_pk_add_f32 v[102:103], v[108:109], v[102:103]
	v_cvt_f32_f16_sdwa v109, v97 dst_sel:DWORD dst_unused:UNUSED_PAD src0_sel:WORD_1
	v_cvt_f32_f16_e32 v108, v97
	v_cvt_f32_f16_sdwa v97, v96 dst_sel:DWORD dst_unused:UNUSED_PAD src0_sel:WORD_1
	v_cvt_f32_f16_e32 v96, v96
	v_pk_add_f32 v[98:99], v[110:111], v[98:99]
	v_pk_add_f32 v[104:105], v[104:105], v[108:109]
	v_mov_b32_e32 v108, v103
	v_mov_b32_e32 v109, v105
	v_pk_add_f32 v[96:97], v[106:107], v[96:97]
	v_mov_b32_e32 v106, v102
	v_mov_b32_e32 v107, v104
	v_pk_mul_f32 v[108:109], v[108:109], v[108:109]
	v_pk_fma_f32 v[100:101], v[112:113], v[112:113], v[100:101]
	v_pk_fma_f32 v[106:107], v[106:107], v[106:107], v[108:109]
	v_mov_b32_e32 v108, v98
	v_mov_b32_e32 v109, v96
	v_mov_b32_e32 v110, v99
	v_mov_b32_e32 v111, v97
	v_pk_fma_f32 v[106:107], v[108:109], v[108:109], v[106:107]
	v_add_f32_e32 v95, v100, v101
	v_pk_fma_f32 v[106:107], v[110:111], v[110:111], v[106:107]
	v_lshl_add_u64 v[34:35], v[34:35], 0, s[12:13]
	v_add_f32_e32 v95, v95, v106
	v_add_f32_e32 v95, v95, v107
	v_mov_b32_e32 v100, v95
	s_nop 1
	v_permlane32_swap_b32 v100, v95
	s_waitcnt lgkmcnt(0)
	v_add_f32_e32 v95, v95, v100
	v_mov_b32_e32 v100, v95
	s_nop 1
	v_permlane16_swap_b32 v100, v95
	s_waitcnt lgkmcnt(0)
	v_add_f32_e32 v95, v95, v100
	s_nop 1
	v_mov_b32_dpp v100, v95 row_ror:8 row_mask:0xf bank_mask:0xf
	s_waitcnt lgkmcnt(0)
	v_add_f32_e32 v95, v95, v100
	s_nop 1
	v_mov_b32_dpp v100, v95 row_half_mirror row_mask:0xf bank_mask:0xf
	s_nop 1
	v_mov_b32_dpp v100, v100 quad_perm:[3,2,1,0] row_mask:0xf bank_mask:0xf
	s_waitcnt lgkmcnt(0)
	v_add_f32_e32 v95, v95, v100
	s_nop 1
	v_mov_b32_dpp v100, v95 quad_perm:[2,3,0,1] row_mask:0xf bank_mask:0xf
	s_waitcnt lgkmcnt(0)
	v_add_f32_e32 v95, v95, v100
	s_nop 1
	v_mov_b32_dpp v100, v95 quad_perm:[1,0,3,2] row_mask:0xf bank_mask:0xf
	s_waitcnt lgkmcnt(0)
	v_add_f32_e32 v95, v95, v100
	v_fmamk_f32 v95, v95, 0x3a800000, v191
	v_cmp_gt_f32_e32 vcc, s18, v95
	v_mul_f32_e32 v100, 0x4b800000, v95
	s_nop 0
	v_cndmask_b32_e32 v95, v95, v100, vcc
	v_rsq_f32_e32 v95, v95
	s_nop 0
	v_mul_f32_e32 v100, 0x45800000, v95
	v_cndmask_b32_e32 v100, v95, v100, vcc
	v_pk_mul_f32 v[84:85], v[84:85], v[100:101] op_sel_hi:[1,0]
	v_pk_mul_f32 v[0:1], v[124:125], v[84:85]
	v_pk_mul_f32 v[84:85], v[90:91], v[100:101] op_sel_hi:[1,0]
	s_nop 0
	v_pk_mul_f32 v[2:3], v[126:127], v[84:85]
	global_store_dwordx4 v[72:73], v[0:3], off
	s_nop 1
	v_pk_mul_f32 v[84:85], v[86:87], v[100:101] op_sel_hi:[1,0]
	v_pk_mul_f32 v[0:1], v[128:129], v[84:85]
	v_pk_mul_f32 v[84:85], v[88:89], v[100:101] op_sel_hi:[1,0]
	s_nop 0
	v_pk_mul_f32 v[2:3], v[130:131], v[84:85]
	global_store_dwordx4 v[72:73], v[0:3], off offset:16
	s_nop 1
	v_pk_mul_f32 v[84:85], v[102:103], v[100:101] op_sel_hi:[1,0]
	v_pk_mul_f32 v[0:1], v[84:85], v[132:133]
	v_pk_mul_f32 v[84:85], v[98:99], v[100:101] op_sel_hi:[1,0]
	s_nop 0
	v_pk_mul_f32 v[2:3], v[84:85], v[134:135]
	global_store_dwordx4 v[72:73], v[0:3], off offset:32
	s_nop 1
	v_pk_mul_f32 v[84:85], v[104:105], v[100:101] op_sel_hi:[1,0]
	v_pk_mul_f32 v[0:1], v[84:85], v[136:137]
	v_pk_mul_f32 v[84:85], v[96:97], v[100:101] op_sel_hi:[1,0]
	s_nop 0
	v_pk_mul_f32 v[2:3], v[84:85], v[138:139]
	global_store_dwordx4 v[72:73], v[0:3], off offset:48
	s_nop 1
	v_mov_b32_e32 v0, v94
	s_andn2_b64 exec, exec, s[10:11]
	s_cbranch_execnz .LBB0_762
